# speedup vs baseline: 1.0070x; 1.0070x over previous
_Z6k_partPKiPKfS2_S2_S2_S2_PiS3_PDF16_S4_S4_:
	s_cmpk_gt_i32 s2, 0xf4
	s_mov_b64 s[4:5], -1
	s_cbranch_scc0 .LBB0_60
	s_cmpk_gt_u32 s2, 0x1f4
	s_cbranch_scc0 .LBB0_53
	s_load_dwordx4 s[4:7], s[0:1], 0x10
	v_lshrrev_b32_e32 v1, 4, v0
	v_and_b32_e32 v3, 15, v0
	v_lshrrev_b32_e32 v2, 1, v0
	v_and_or_b32 v1, v1, 48, v3
	v_and_b32_e32 v4, 0x78, v2
	v_lshl_add_u32 v1, v1, 6, v4
	v_lshlrev_b32_e32 v4, 2, v1
	v_mov_b32_e32 v5, 0
	v_and_b32_e32 v8, 0x60, v2
	s_waitcnt lgkmcnt(0)
	v_lshl_add_u64 v[6:7], s[4:5], 0, v[4:5]
	v_subrev_u32_e32 v4, 64, v1
	v_lshl_add_u64 v[4:5], v[4:5], 2, s[6:7]
	v_cmp_gt_u32_e32 vcc, 64, v8
	s_load_dwordx2 s[4:5], s[0:1], 0x48
	s_movk_i32 s3, 0x80
	v_cndmask_b32_e32 v13, v5, v7, vcc
	v_cndmask_b32_e32 v12, v4, v6, vcc
	global_load_dwordx4 v[4:7], v[12:13], off offset:16
	global_load_dwordx4 v[8:11], v[12:13], off
	v_lshlrev_b32_e32 v1, 4, v0
	v_cmp_gt_u32_e32 vcc, s3, v0
	s_waitcnt vmcnt(1)
	v_cvt_pk_f16_f32 v7, v6, v7
	v_cvt_pk_f16_f32 v6, v4, v5
	s_waitcnt vmcnt(0)
	v_cvt_pk_f16_f32 v5, v10, v11
	v_cvt_pk_f16_f32 v4, v8, v9
	s_waitcnt lgkmcnt(0)
	global_store_dwordx4 v1, v[4:7], s[4:5] sc1
	s_and_saveexec_b64 s[6:7], vcc
	s_cbranch_execz .LBB0_52
	s_load_dwordx4 s[8:11], s[0:1], 0x20
	v_lshrrev_b32_e32 v4, 2, v0
	v_and_b32_e32 v4, 12, v4
	v_and_or_b32 v2, v2, 32, v4
	v_cmp_lt_u32_e64 s[4:5], 1, v3
	v_cmp_gt_u32_e32 vcc, 4, v3
	v_lshlrev_b32_e32 v8, 6, v3
	s_and_saveexec_b64 s[12:13], s[4:5]
	s_xor_b64 s[12:13], exec, s[12:13]
	s_cbranch_execz .LBB0_7
	v_mov_b32_e32 v6, 0
	s_and_saveexec_b64 s[14:15], vcc
	s_cbranch_execz .LBB0_6
	v_add_lshl_u32 v3, v2, v8, 2
	s_waitcnt lgkmcnt(0)
	global_load_dword v6, v3, s[10:11] offset:-512

.LBB0_51:
	s_or_b64 exec, exec, s[4:5]
	s_waitcnt vmcnt(0)
	v_cvt_pk_f16_f32 v5, v13, v3
	v_cvt_pk_f16_f32 v4, v11, v12
	v_cvt_pk_f16_f32 v3, v8, v10
	v_cvt_pk_f16_f32 v2, v6, v7
	s_waitcnt lgkmcnt(0)
	global_store_dwordx4 v1, v[2:5], s[12:13] sc1

.LBB0_56:
	s_or_b64 exec, exec, s[8:9]
	s_waitcnt vmcnt(4)
	v_cvt_pk_f16_f32 v5, v4, v5
	v_cvt_pk_f16_f32 v4, v2, v3
	v_lshl_add_u64 v[2:3], v[32:33], 3, s[4:5]
	global_store_dwordx2 v[2:3], v[4:5], off sc1
	s_waitcnt vmcnt(4)
	v_cvt_pk_f16_f32 v3, v20, v21
	v_cvt_pk_f16_f32 v2, v18, v19
	v_lshl_add_u64 v[4:5], v[38:39], 3, s[4:5]
	global_store_dwordx2 v[4:5], v[2:3], off sc1
	s_waitcnt vmcnt(4)
	v_cvt_pk_f16_f32 v3, v8, v9
	v_cvt_pk_f16_f32 v2, v6, v7
	v_lshl_add_u64 v[4:5], v[34:35], 3, s[4:5]
	global_store_dwordx2 v[4:5], v[2:3], off sc1
	s_waitcnt vmcnt(4)
	v_cvt_pk_f16_f32 v3, v24, v25
	v_cvt_pk_f16_f32 v2, v22, v23
	v_lshl_add_u64 v[4:5], v[40:41], 3, s[4:5]
	v_cvt_pk_f16_f32 v17, v16, v17
	v_cvt_pk_f16_f32 v16, v14, v15
	v_lshl_add_u64 v[14:15], v[30:31], 3, s[4:5]
	global_store_dwordx2 v[4:5], v[2:3], off sc1
	s_waitcnt vmcnt(4)
	v_cvt_pk_f16_f32 v3, v12, v13
	v_cvt_pk_f16_f32 v2, v10, v11
	v_lshl_add_u64 v[4:5], v[36:37], 3, s[4:5]
	global_store_dwordx2 v[14:15], v[16:17], off sc1
	global_store_dwordx2 v[4:5], v[2:3], off sc1
	s_and_saveexec_b64 s[6:7], vcc
	s_cbranch_execz .LBB0_58
	v_mov_b32_e32 v43, 0
	v_cvt_pk_f16_f32 v3, v28, v29
	v_cvt_pk_f16_f32 v2, v26, v27
	v_lshl_add_u64 v[4:5], v[42:43], 3, s[4:5]
	global_store_dwordx2 v[4:5], v[2:3], off sc1

.LBB0_89:
	s_or_b64 exec, exec, s[10:11]
	v_sub_u32_e32 v15, v16, v15
	s_movk_i32 s0, 0x3fe
	v_add_u32_e32 v15, v15, v17
	v_cmp_gt_u32_e64 s[0:1], s0, v0
	ds_write_b32 v14, v15
	s_waitcnt lgkmcnt(0)
	s_barrier
	s_and_saveexec_b64 s[10:11], s[0:1]
	s_cbranch_execz .LBB0_99
	ds_read_b32 v16, v14
	s_mulk_i32 s2, 0x3fe
	v_add_u32_e32 v14, s2, v0
	v_ashrrev_i32_e32 v15, 31, v14
	v_lshl_add_u64 v[14:15], v[14:15], 2, s[14:15]
	s_waitcnt lgkmcnt(0)
	global_store_dword v[14:15], v16, off sc1
	s_or_b64 exec, exec, s[10:11]
	s_and_saveexec_b64 s[0:1], vcc
	s_cbranch_execnz .LBB0_100

.LBB0_97:
	ds_read_b32 v4, v1
	v_add_u32_e32 v0, 0x400, v0
	v_cmp_le_u32_e32 vcc, s4, v0
	v_add_u32_e32 v1, 0x1000, v1
	s_or_b64 s[0:1], vcc, s[0:1]
	s_waitcnt lgkmcnt(0)
	global_store_dword v[2:3], v4, off sc1
	v_lshl_add_u64 v[2:3], v[2:3], 0, s[2:3]
	s_andn2_b64 exec, exec, s[0:1]
	s_cbranch_execnz .LBB0_97
